# adds: GU source-row table and LN2 modulation-vector staging request all their loads before the first wait (were chains of 24 / 14 dependent load-wait steps)
# baseline (speedup 1.0000x reference)
; #define LAS __attribute__((address_space(3)))
; __device__ __forceinline__ void lds_barrier() { asm volatile("s_waitcnt lgkmcnt(0)" ::: "memory"); __builtin_amdgcn_s_barrier(); asm volatile("" ::: "memory"); }
;     __device__ __forceinline__ bool next(int i, Unit& u) const {
;         const int t = (i / nN) * G + c; if (t >= ntiles) return false;
;         u.pn = i % nN; const unsigned pk = (unsigned)__builtin_amdgcn_readfirstlane((int)tiles[t]); u.e = (int)(pk >> 16); u.pm = (int)(pk & 0xffffu); return true;
;     }
; __global__ void __launch_bounds__(NWAVES * 64, 2) mk_fwd(Args args) {
;     ...
;                 {
;                     LAS int* LT = (LAS int*)(F.lds + RING_BYTES); pg8::Unit uu;
; #pragma unroll 1
;                     for (int i = 0; i < 24 && S.next(i, uu); ++i) if (F.tid < 256) LT[i * 256 + F.tid] = S.arow_g(uu, F.tid);
;                     lds_barrier(); }
.LBB0_1580:
	s_or_b64 exec, exec, s[0:1]
	v_readlane_b32 s4, v252, 4
	v_mov_b32_e32 v2, v200
	v_readlane_b32 s19, v252, 10
	s_mov_b64 s[0:1], 0
	v_readlane_b32 s6, v252, 6
	s_waitcnt lgkmcnt(0)
	s_barrier
	v_readlane_b32 s7, v252, 7
	s_add_u32 s9, s6, s0
	s_addc_u32 s12, s7, s1
	v_lshl_add_u32 v0, s19, 6, v2
	s_add_u32 s2, s9, 0xd00000
	s_movk_i32 s4, 0x100
	s_addc_u32 s3, s12, 0
	v_cmp_gt_i32_e64 s[36:37], s4, v0
	s_lshl_b32 s4, s19, 8
	s_add_i32 s4, s4, 0
	s_add_i32 s4, s4, 0x20000
	v_readfirstlane_b32 s8, v4
	v_add_u32_e32 v1, 0xfffb8000, v0
	v_lshl_add_u32 v2, v2, 2, s4
	s_mov_b32 s13, 0
	v_readlane_b32 s5, v252, 5
	v_readlane_b32 s4, v254, 12
	v_mov_b32_e32 v5, s4
	v_mad_u32_u24 v5, v200, s70, v5
	v_min_u32_e32 v5, 0x5ff, v5
	v_lshlrev_b32_e32 v5, 2, v5
	v_add_u32_e32 v5, 0x26400, v5
	ds_read_b32 v6, v5
	s_mov_b32 s5, s4
	s_and_saveexec_b64 s[16:17], s[36:37]
	s_waitcnt lgkmcnt(0)
	s_movk_i32 s13, 0
	s_cmp_ge_i32 s5, s8
	s_cbranch_scc1 .Lltok_wr
	v_readlane_b32 s6, v6, 0
	s_nop 0
	s_lshr_b32 s7, s6, 16
	v_writelane_b32 v255, s7, 3
	s_and_b32 s6, s6, 0xffff
	v_writelane_b32 v255, s6, 4
	s_lshl_b32 s14, s6, 8
	s_cmp_lt_i32 s7, 64
	s_cbranch_scc0 .Lltok_sh0
	v_add_lshl_u32 v32, v0, s14, 2
	global_load_dword v16, v32, s[2:3]
	s_branch .Lltok_n0
.Lltok_sh0:
	v_add_u32_e32 v16, s14, v1
.Lltok_n0:
	s_add_i32 s5, s5, s70
	s_movk_i32 s13, 1
	s_cmp_ge_i32 s5, s8
	s_cbranch_scc1 .Lltok_wr
	v_readlane_b32 s6, v6, 1
	s_nop 0
	s_lshr_b32 s7, s6, 16
	v_writelane_b32 v255, s7, 3
	s_and_b32 s6, s6, 0xffff
	v_writelane_b32 v255, s6, 4
	s_lshl_b32 s14, s6, 8
	s_cmp_lt_i32 s7, 64
	s_cbranch_scc0 .Lltok_sh1
	v_add_lshl_u32 v33, v0, s14, 2
	global_load_dword v17, v33, s[2:3]
	s_branch .Lltok_n1
.Lltok_sh1:
	v_add_u32_e32 v17, s14, v1
.Lltok_n1:
	s_add_i32 s5, s5, s70
	s_movk_i32 s13, 2
	s_cmp_ge_i32 s5, s8
	s_cbranch_scc1 .Lltok_wr
	v_readlane_b32 s6, v6, 2
	s_nop 0
	s_lshr_b32 s7, s6, 16
	v_writelane_b32 v255, s7, 3
	s_and_b32 s6, s6, 0xffff
	v_writelane_b32 v255, s6, 4
	s_lshl_b32 s14, s6, 8
	s_cmp_lt_i32 s7, 64
	s_cbranch_scc0 .Lltok_sh2
	v_add_lshl_u32 v34, v0, s14, 2
	global_load_dword v18, v34, s[2:3]
	s_branch .Lltok_n2
.Lltok_sh2:
	v_add_u32_e32 v18, s14, v1
.Lltok_n2:
	s_add_i32 s5, s5, s70
	s_movk_i32 s13, 3
	s_cmp_ge_i32 s5, s8
	s_cbranch_scc1 .Lltok_wr
	v_readlane_b32 s6, v6, 3
	s_nop 0
	s_lshr_b32 s7, s6, 16
	v_writelane_b32 v255, s7, 3
	s_and_b32 s6, s6, 0xffff
	v_writelane_b32 v255, s6, 4
	s_lshl_b32 s14, s6, 8
	s_cmp_lt_i32 s7, 64
	s_cbranch_scc0 .Lltok_sh3
	v_add_lshl_u32 v35, v0, s14, 2
	global_load_dword v19, v35, s[2:3]
	s_branch .Lltok_n3
.Lltok_sh3:
	v_add_u32_e32 v19, s14, v1
.Lltok_n3:
	s_add_i32 s5, s5, s70
	s_movk_i32 s13, 4
	s_cmp_ge_i32 s5, s8
	s_cbranch_scc1 .Lltok_wr
	v_readlane_b32 s6, v6, 4
	s_nop 0
	s_lshr_b32 s7, s6, 16
	v_writelane_b32 v255, s7, 3
	s_and_b32 s6, s6, 0xffff
	v_writelane_b32 v255, s6, 4
	s_lshl_b32 s14, s6, 8
	s_cmp_lt_i32 s7, 64
	s_cbranch_scc0 .Lltok_sh4
	v_add_lshl_u32 v36, v0, s14, 2
	global_load_dword v20, v36, s[2:3]
	s_branch .Lltok_n4
.Lltok_sh4:
	v_add_u32_e32 v20, s14, v1
.Lltok_n4:
	s_add_i32 s5, s5, s70
	s_movk_i32 s13, 5
	s_cmp_ge_i32 s5, s8
	s_cbranch_scc1 .Lltok_wr
	v_readlane_b32 s6, v6, 5
	s_nop 0
	s_lshr_b32 s7, s6, 16
	v_writelane_b32 v255, s7, 3
	s_and_b32 s6, s6, 0xffff
	v_writelane_b32 v255, s6, 4
	s_lshl_b32 s14, s6, 8
	s_cmp_lt_i32 s7, 64
	s_cbranch_scc0 .Lltok_sh5
	v_add_lshl_u32 v37, v0, s14, 2
	global_load_dword v21, v37, s[2:3]
	s_branch .Lltok_n5
.Lltok_sh5:
	v_add_u32_e32 v21, s14, v1
.Lltok_n5:
	s_add_i32 s5, s5, s70
	s_movk_i32 s13, 6
	s_cmp_ge_i32 s5, s8
	s_cbranch_scc1 .Lltok_wr
	v_readlane_b32 s6, v6, 6
	s_nop 0
	s_lshr_b32 s7, s6, 16
	v_writelane_b32 v255, s7, 3
	s_and_b32 s6, s6, 0xffff
	v_writelane_b32 v255, s6, 4
	s_lshl_b32 s14, s6, 8
	s_cmp_lt_i32 s7, 64
	s_cbranch_scc0 .Lltok_sh6
	v_add_lshl_u32 v38, v0, s14, 2
	global_load_dword v22, v38, s[2:3]
	s_branch .Lltok_n6
; __device__ __forceinline__ void lds_barrier() { asm volatile("s_waitcnt lgkmcnt(0)" ::: "memory"); __builtin_amdgcn_s_barrier(); asm volatile("" ::: "memory"); }
; __global__ void __launch_bounds__(NWAVES * 64, 2) mk_fwd(Args args) {
;     ...
;                     for (int i = 0; i < 24 && S.next(i, uu); ++i) if (F.tid < 256) LT[i * 256 + F.tid] = S.arow_g(uu, F.tid);
;                     lds_barrier(); }
.Lltok_sh6:
	v_add_u32_e32 v22, s14, v1
.Lltok_n6:
	s_add_i32 s5, s5, s70
	s_movk_i32 s13, 7
	s_cmp_ge_i32 s5, s8
	s_cbranch_scc1 .Lltok_wr
	v_readlane_b32 s6, v6, 7
	s_nop 0
	s_lshr_b32 s7, s6, 16
	v_writelane_b32 v255, s7, 3
	s_and_b32 s6, s6, 0xffff
	v_writelane_b32 v255, s6, 4
	s_lshl_b32 s14, s6, 8
	s_cmp_lt_i32 s7, 64
	s_cbranch_scc0 .Lltok_sh7
	v_add_lshl_u32 v39, v0, s14, 2
	global_load_dword v23, v39, s[2:3]
	s_branch .Lltok_n7
.Lltok_sh7:
	v_add_u32_e32 v23, s14, v1
.Lltok_n7:
	s_add_i32 s5, s5, s70
	s_movk_i32 s13, 8
	s_cmp_ge_i32 s5, s8
	s_cbranch_scc1 .Lltok_wr
	v_readlane_b32 s6, v6, 8
	s_nop 0
	s_lshr_b32 s7, s6, 16
	v_writelane_b32 v255, s7, 3
	s_and_b32 s6, s6, 0xffff
	v_writelane_b32 v255, s6, 4
	s_lshl_b32 s14, s6, 8
	s_cmp_lt_i32 s7, 64
	s_cbranch_scc0 .Lltok_sh8
	v_add_lshl_u32 v40, v0, s14, 2
	global_load_dword v24, v40, s[2:3]
	s_branch .Lltok_n8
.Lltok_sh8:
	v_add_u32_e32 v24, s14, v1
.Lltok_n8:
	s_add_i32 s5, s5, s70
	s_movk_i32 s13, 9
	s_cmp_ge_i32 s5, s8
	s_cbranch_scc1 .Lltok_wr
	v_readlane_b32 s6, v6, 9
	s_nop 0
	s_lshr_b32 s7, s6, 16
	v_writelane_b32 v255, s7, 3
	s_and_b32 s6, s6, 0xffff
	v_writelane_b32 v255, s6, 4
	s_lshl_b32 s14, s6, 8
	s_cmp_lt_i32 s7, 64
	s_cbranch_scc0 .Lltok_sh9
	v_add_lshl_u32 v41, v0, s14, 2
	global_load_dword v25, v41, s[2:3]
	s_branch .Lltok_n9
.Lltok_sh9:
	v_add_u32_e32 v25, s14, v1
.Lltok_n9:
	s_add_i32 s5, s5, s70
	s_movk_i32 s13, 10
	s_cmp_ge_i32 s5, s8
	s_cbranch_scc1 .Lltok_wr
	v_readlane_b32 s6, v6, 10
	s_nop 0
	s_lshr_b32 s7, s6, 16
	v_writelane_b32 v255, s7, 3
	s_and_b32 s6, s6, 0xffff
	v_writelane_b32 v255, s6, 4
	s_lshl_b32 s14, s6, 8
	s_cmp_lt_i32 s7, 64
	s_cbranch_scc0 .Lltok_sh10
	v_add_lshl_u32 v42, v0, s14, 2
	global_load_dword v26, v42, s[2:3]
	s_branch .Lltok_n10
.Lltok_sh10:
	v_add_u32_e32 v26, s14, v1
.Lltok_n10:
	s_add_i32 s5, s5, s70
	s_movk_i32 s13, 11
	s_cmp_ge_i32 s5, s8
	s_cbranch_scc1 .Lltok_wr
	v_readlane_b32 s6, v6, 11
	s_nop 0
	s_lshr_b32 s7, s6, 16
	v_writelane_b32 v255, s7, 3
	s_and_b32 s6, s6, 0xffff
	v_writelane_b32 v255, s6, 4
	s_lshl_b32 s14, s6, 8
	s_cmp_lt_i32 s7, 64
	s_cbranch_scc0 .Lltok_sh11
	v_add_lshl_u32 v43, v0, s14, 2
	global_load_dword v27, v43, s[2:3]
	s_branch .Lltok_n11
.Lltok_sh11:
	v_add_u32_e32 v27, s14, v1
.Lltok_n11:
	s_add_i32 s5, s5, s70
	s_movk_i32 s13, 12
.Lltok_wr:
	s_waitcnt vmcnt(0)
	s_cmp_le_u32 s13, 0
	s_cbranch_scc1 .Lltok_done
	ds_write_b32 v2, v16
	ds_write_b32 v2, v16 offset:1024
	s_cmp_le_u32 s13, 1
	s_cbranch_scc1 .Lltok_done
	ds_write_b32 v2, v17 offset:2048
	ds_write_b32 v2, v17 offset:3072
	s_cmp_le_u32 s13, 2
	s_cbranch_scc1 .Lltok_done
	ds_write_b32 v2, v18 offset:4096
	ds_write_b32 v2, v18 offset:5120
	s_cmp_le_u32 s13, 3
	s_cbranch_scc1 .Lltok_done
	ds_write_b32 v2, v19 offset:6144
	ds_write_b32 v2, v19 offset:7168
	s_cmp_le_u32 s13, 4
	s_cbranch_scc1 .Lltok_done
	ds_write_b32 v2, v20 offset:8192
	ds_write_b32 v2, v20 offset:9216
	s_cmp_le_u32 s13, 5
	s_cbranch_scc1 .Lltok_done
	ds_write_b32 v2, v21 offset:10240
	ds_write_b32 v2, v21 offset:11264
	s_cmp_le_u32 s13, 6
	s_cbranch_scc1 .Lltok_done
	ds_write_b32 v2, v22 offset:12288
	ds_write_b32 v2, v22 offset:13312
	s_cmp_le_u32 s13, 7
	s_cbranch_scc1 .Lltok_done
	ds_write_b32 v2, v23 offset:14336
	ds_write_b32 v2, v23 offset:15360
	s_cmp_le_u32 s13, 8
	s_cbranch_scc1 .Lltok_done
	ds_write_b32 v2, v24 offset:16384
	ds_write_b32 v2, v24 offset:17408
	s_cmp_le_u32 s13, 9
	s_cbranch_scc1 .Lltok_done
	ds_write_b32 v2, v25 offset:18432
	ds_write_b32 v2, v25 offset:19456
	s_cmp_le_u32 s13, 10
	s_cbranch_scc1 .Lltok_done
	ds_write_b32 v2, v26 offset:20480
	ds_write_b32 v2, v26 offset:21504
	s_cmp_le_u32 s13, 11
	s_cbranch_scc1 .Lltok_done
	ds_write_b32 v2, v27 offset:22528
	ds_write_b32 v2, v27 offset:23552
.Lltok_done:
	s_mov_b64 exec, s[16:17]

; #define LAS __attribute__((address_space(3)))
; __device__ __forceinline__ const float* modv(const Frame& F, int l, int r, int k) { return (const float*)(F.ws + WS_MODV) + ((size_t)(l * 9 + r) * 6 + k) * 1024; }
; __device__ __forceinline__ void phase_ln2(Frame& F0, const Args& A, int l, bool have_moe) {
;     ...
;     for (int i = F.tid; i < 27 * 256; i += 512) { const int r = i / 768, k = (i / 256) % 3, c = (i & 255) * 4;
;         const f32x4 v = (k == 0) ? *(const f32x4*)(modv(F, l, r, 5) + c) : (last ? (f32x4){0.f, 0.f, 0.f, 0.f} : *(const f32x4*)(modv(F, l + 1, r, k == 1 ? 1 : 0) + c));
;         *(LAS f32x4*)(MV + (r * 3 + k) * 1024 + c) = v; }
.LBB0_1693:
	s_or_b64 exec, exec, s[0:1]
	v_readlane_b32 s18, v252, 10
	v_mov_b32_e32 v156, v200
	v_readlane_b32 s4, v252, 4
	s_waitcnt lgkmcnt(0)
	s_barrier
	s_lshl_b32 s19, s18, 6
	s_mov_b64 s[2:3], 0
	v_readlane_b32 s5, v252, 5
	v_readlane_b32 s6, v252, 6
	v_readlane_b32 s7, v252, 7
	s_add_u32 s0, s6, s2
	s_mov_b32 s4, s91
	s_mov_b32 s5, s2
	s_addc_u32 s1, s7, s3
	s_ashr_i64 s[4:5], s[4:5], 29
	v_readlane_b32 s6, v252, 0
	v_readlane_b32 s7, v252, 1
	s_add_u32 s4, s6, s4
	s_addc_u32 s5, s7, s5
	s_load_dwordx4 s[36:39], s[4:5], 0x40
	s_waitcnt lgkmcnt(0)
	s_barrier
	v_add_u32_e32 v5, s19, v156
	s_movk_i32 s4, 0x1b00
	v_lshlrev_b32_e32 v0, 2, v156
	v_cmp_gt_i32_e32 vcc, s4, v5
	v_lshl_add_u32 v4, s18, 8, v0
	s_and_saveexec_b64 s[4:5], vcc
	s_cbranch_execz .LBB0_1704
	v_and_b32_e32 v10, 0xff, v5
	v_lshlrev_b32_e32 v10, 4, v10
	v_lshlrev_b32_e32 v11, 4, v5
	v_add_u32_e32 v12, 0x10000, v11
	s_add_u32 s8, s0, 0x100000
	s_addc_u32 s9, s1, 0
	v_readlane_b32 s6, v254, 58
	v_readlane_b32 s22, v254, 50
	v_readlane_b32 s23, v254, 51
	s_lshr_b32 s7, s18, 2
	s_add_i32 s12, s7, 0
	s_mul_hi_u32 s13, s12, 0x55555556
	s_mul_i32 s14, s13, 3
	s_sub_i32 s14, s12, s14
	s_add_i32 s15, s13, s6
	s_cmp_eq_u32 s14, 0
	s_cbranch_scc0 .Lln2st_k0
	s_mul_i32 s16, s15, 0x6000
	s_add_u32 s16, s16, 0x105000
	s_add_u32 s20, s0, s16
	s_addc_u32 s21, s1, 0
	global_load_dwordx4 v[16:19], v10, s[20:21]
	s_branch .Lln2st_n0
.Lln2st_k0:
	v_mov_b32_e32 v16, 0
	v_mov_b32_e32 v17, 0
	v_mov_b32_e32 v18, 0
	v_mov_b32_e32 v19, 0
	s_and_b64 vcc, exec, s[22:23]
	s_cbranch_vccz .Lln2st_n0
	s_add_i32 s15, s15, 9
	s_mul_i32 s16, s15, 6
	s_cmp_eq_u32 s14, 1
	s_cselect_b32 s17, 1, 0
	s_or_b32 s16, s16, s17
	s_lshl_b32 s16, s16, 12
	s_add_u32 s20, s8, s16
	s_addc_u32 s21, s9, 0
	global_load_dwordx4 v[16:19], v10, s[20:21]
.Lln2st_n0:
	s_add_i32 s12, s7, 2
	s_mul_hi_u32 s13, s12, 0x55555556
	s_mul_i32 s14, s13, 3
	s_sub_i32 s14, s12, s14
	s_add_i32 s15, s13, s6
	s_cmp_eq_u32 s14, 0
	s_cbranch_scc0 .Lln2st_k1
	s_mul_i32 s16, s15, 0x6000
	s_add_u32 s16, s16, 0x105000
	s_add_u32 s20, s0, s16
	s_addc_u32 s21, s1, 0
	global_load_dwordx4 v[20:23], v10, s[20:21]
	s_branch .Lln2st_n1
.Lln2st_k1:
	v_mov_b32_e32 v20, 0
	v_mov_b32_e32 v21, 0
	v_mov_b32_e32 v22, 0
	v_mov_b32_e32 v23, 0
	s_and_b64 vcc, exec, s[22:23]
	s_cbranch_vccz .Lln2st_n1
	s_add_i32 s15, s15, 9
	s_mul_i32 s16, s15, 6
	s_cmp_eq_u32 s14, 1
	s_cselect_b32 s17, 1, 0
	s_or_b32 s16, s16, s17
	s_lshl_b32 s16, s16, 12
	s_add_u32 s20, s8, s16
	s_addc_u32 s21, s9, 0
	global_load_dwordx4 v[20:23], v10, s[20:21]
.Lln2st_n1:
	s_add_i32 s12, s7, 4
	s_mul_hi_u32 s13, s12, 0x55555556
	s_mul_i32 s14, s13, 3
	s_sub_i32 s14, s12, s14
	s_add_i32 s15, s13, s6
	s_cmp_eq_u32 s14, 0
	s_cbranch_scc0 .Lln2st_k2
	s_mul_i32 s16, s15, 0x6000
	s_add_u32 s16, s16, 0x105000
	s_add_u32 s20, s0, s16
	s_addc_u32 s21, s1, 0
	global_load_dwordx4 v[24:27], v10, s[20:21]
	s_branch .Lln2st_n2
.Lln2st_k2:
	v_mov_b32_e32 v24, 0
	v_mov_b32_e32 v25, 0
	v_mov_b32_e32 v26, 0
	v_mov_b32_e32 v27, 0
	s_and_b64 vcc, exec, s[22:23]
	s_cbranch_vccz .Lln2st_n2
	s_add_i32 s15, s15, 9
	s_mul_i32 s16, s15, 6
	s_cmp_eq_u32 s14, 1
	s_cselect_b32 s17, 1, 0
	s_or_b32 s16, s16, s17
	s_lshl_b32 s16, s16, 12
	s_add_u32 s20, s8, s16
	s_addc_u32 s21, s9, 0
	global_load_dwordx4 v[24:27], v10, s[20:21]
.Lln2st_n2:
	s_add_i32 s12, s7, 6
	s_mul_hi_u32 s13, s12, 0x55555556
	s_mul_i32 s14, s13, 3
	s_sub_i32 s14, s12, s14
	s_add_i32 s15, s13, s6
	s_cmp_eq_u32 s14, 0
	s_cbranch_scc0 .Lln2st_k3
	s_mul_i32 s16, s15, 0x6000
	s_add_u32 s16, s16, 0x105000
	s_add_u32 s20, s0, s16
	s_addc_u32 s21, s1, 0
	global_load_dwordx4 v[28:31], v10, s[20:21]
	s_branch .Lln2st_n3
.Lln2st_k3:
	v_mov_b32_e32 v28, 0
	v_mov_b32_e32 v29, 0
	v_mov_b32_e32 v30, 0
	v_mov_b32_e32 v31, 0
	s_and_b64 vcc, exec, s[22:23]
	s_cbranch_vccz .Lln2st_n3
	s_add_i32 s15, s15, 9
	s_mul_i32 s16, s15, 6
	s_cmp_eq_u32 s14, 1
	s_cselect_b32 s17, 1, 0
	s_or_b32 s16, s16, s17
	s_lshl_b32 s16, s16, 12
	s_add_u32 s20, s8, s16
	s_addc_u32 s21, s9, 0
	global_load_dwordx4 v[28:31], v10, s[20:21]
.Lln2st_n3:
	s_add_i32 s12, s7, 8
	s_mul_hi_u32 s13, s12, 0x55555556
	s_mul_i32 s14, s13, 3
	s_sub_i32 s14, s12, s14
	s_add_i32 s15, s13, s6
	s_cmp_eq_u32 s14, 0
	s_cbranch_scc0 .Lln2st_k4
	s_mul_i32 s16, s15, 0x6000
	s_add_u32 s16, s16, 0x105000
	s_add_u32 s20, s0, s16
	s_addc_u32 s21, s1, 0
	global_load_dwordx4 v[32:35], v10, s[20:21]
	s_branch .Lln2st_n4
.Lln2st_k4:
	v_mov_b32_e32 v32, 0
	v_mov_b32_e32 v33, 0
	v_mov_b32_e32 v34, 0
	v_mov_b32_e32 v35, 0
	s_and_b64 vcc, exec, s[22:23]
	s_cbranch_vccz .Lln2st_n4
	s_add_i32 s15, s15, 9
	s_mul_i32 s16, s15, 6
	s_cmp_eq_u32 s14, 1
	s_cselect_b32 s17, 1, 0
	s_or_b32 s16, s16, s17
	s_lshl_b32 s16, s16, 12
	s_add_u32 s20, s8, s16
	s_addc_u32 s21, s9, 0
	global_load_dwordx4 v[32:35], v10, s[20:21]
.Lln2st_n4:
	s_add_i32 s12, s7, 10
	s_mul_hi_u32 s13, s12, 0x55555556
	s_mul_i32 s14, s13, 3
	s_sub_i32 s14, s12, s14
	s_add_i32 s15, s13, s6
	s_cmp_eq_u32 s14, 0
	s_cbranch_scc0 .Lln2st_k5
	s_mul_i32 s16, s15, 0x6000
	s_add_u32 s16, s16, 0x105000
	s_add_u32 s20, s0, s16
	s_addc_u32 s21, s1, 0
	global_load_dwordx4 v[36:39], v10, s[20:21]
	s_branch .Lln2st_n5
.Lln2st_k5:
	v_mov_b32_e32 v36, 0
	v_mov_b32_e32 v37, 0
	v_mov_b32_e32 v38, 0
	v_mov_b32_e32 v39, 0
	s_and_b64 vcc, exec, s[22:23]
	s_cbranch_vccz .Lln2st_n5
	s_add_i32 s15, s15, 9
	s_mul_i32 s16, s15, 6
	s_cmp_eq_u32 s14, 1
	s_cselect_b32 s17, 1, 0
	s_or_b32 s16, s16, s17
	s_lshl_b32 s16, s16, 12
	s_add_u32 s20, s8, s16
	s_addc_u32 s21, s9, 0
	global_load_dwordx4 v[36:39], v10, s[20:21]
; #define LAS __attribute__((address_space(3)))
; __device__ __forceinline__ const float* modv(const Frame& F, int l, int r, int k) { return (const float*)(F.ws + WS_MODV) + ((size_t)(l * 9 + r) * 6 + k) * 1024; }
; __device__ __forceinline__ void phase_ln2(Frame& F0, const Args& A, int l, bool have_moe) {
;     ...
;     for (int i = F.tid; i < 27 * 256; i += 512) { const int r = i / 768, k = (i / 256) % 3, c = (i & 255) * 4;
;         const f32x4 v = (k == 0) ? *(const f32x4*)(modv(F, l, r, 5) + c) : (last ? (f32x4){0.f, 0.f, 0.f, 0.f} : *(const f32x4*)(modv(F, l + 1, r, k == 1 ? 1 : 0) + c));
;         *(LAS f32x4*)(MV + (r * 3 + k) * 1024 + c) = v; }
.Lln2st_n5:
	s_add_i32 s12, s7, 12
	s_mul_hi_u32 s13, s12, 0x55555556
	s_mul_i32 s14, s13, 3
	s_sub_i32 s14, s12, s14
	s_add_i32 s15, s13, s6
	s_cmp_eq_u32 s14, 0
	s_cbranch_scc0 .Lln2st_k6
	s_mul_i32 s16, s15, 0x6000
	s_add_u32 s16, s16, 0x105000
	s_add_u32 s20, s0, s16
	s_addc_u32 s21, s1, 0
	global_load_dwordx4 v[40:43], v10, s[20:21]
	s_branch .Lln2st_n6
.Lln2st_k6:
	v_mov_b32_e32 v40, 0
	v_mov_b32_e32 v41, 0
	v_mov_b32_e32 v42, 0
	v_mov_b32_e32 v43, 0
	s_and_b64 vcc, exec, s[22:23]
	s_cbranch_vccz .Lln2st_n6
	s_add_i32 s15, s15, 9
	s_mul_i32 s16, s15, 6
	s_cmp_eq_u32 s14, 1
	s_cselect_b32 s17, 1, 0
	s_or_b32 s16, s16, s17
	s_lshl_b32 s16, s16, 12
	s_add_u32 s20, s8, s16
	s_addc_u32 s21, s9, 0
	global_load_dwordx4 v[40:43], v10, s[20:21]
.Lln2st_n6:
	s_add_i32 s12, s7, 14
	s_mul_hi_u32 s13, s12, 0x55555556
	s_mul_i32 s14, s13, 3
	s_sub_i32 s14, s12, s14
	s_add_i32 s15, s13, s6
	s_cmp_eq_u32 s14, 0
	s_cbranch_scc0 .Lln2st_k7
	s_mul_i32 s16, s15, 0x6000
	s_add_u32 s16, s16, 0x105000
	s_add_u32 s20, s0, s16
	s_addc_u32 s21, s1, 0
	global_load_dwordx4 v[44:47], v10, s[20:21]
	s_branch .Lln2st_n7
.Lln2st_k7:
	v_mov_b32_e32 v44, 0
	v_mov_b32_e32 v45, 0
	v_mov_b32_e32 v46, 0
	v_mov_b32_e32 v47, 0
	s_and_b64 vcc, exec, s[22:23]
	s_cbranch_vccz .Lln2st_n7
	s_add_i32 s15, s15, 9
	s_mul_i32 s16, s15, 6
	s_cmp_eq_u32 s14, 1
	s_cselect_b32 s17, 1, 0
	s_or_b32 s16, s16, s17
	s_lshl_b32 s16, s16, 12
	s_add_u32 s20, s8, s16
	s_addc_u32 s21, s9, 0
	global_load_dwordx4 v[44:47], v10, s[20:21]
.Lln2st_n7:
	s_add_i32 s12, s7, 16
	s_mul_hi_u32 s13, s12, 0x55555556
	s_mul_i32 s14, s13, 3
	s_sub_i32 s14, s12, s14
	s_add_i32 s15, s13, s6
	s_cmp_eq_u32 s14, 0
	s_cbranch_scc0 .Lln2st_k8
	s_mul_i32 s16, s15, 0x6000
	s_add_u32 s16, s16, 0x105000
	s_add_u32 s20, s0, s16
	s_addc_u32 s21, s1, 0
	global_load_dwordx4 v[48:51], v10, s[20:21]
	s_branch .Lln2st_n8
.Lln2st_k8:
	v_mov_b32_e32 v48, 0
	v_mov_b32_e32 v49, 0
	v_mov_b32_e32 v50, 0
	v_mov_b32_e32 v51, 0
	s_and_b64 vcc, exec, s[22:23]
	s_cbranch_vccz .Lln2st_n8
	s_add_i32 s15, s15, 9
	s_mul_i32 s16, s15, 6
	s_cmp_eq_u32 s14, 1
	s_cselect_b32 s17, 1, 0
	s_or_b32 s16, s16, s17
	s_lshl_b32 s16, s16, 12
	s_add_u32 s20, s8, s16
	s_addc_u32 s21, s9, 0
	global_load_dwordx4 v[48:51], v10, s[20:21]
.Lln2st_n8:
	s_add_i32 s12, s7, 18
	s_mul_hi_u32 s13, s12, 0x55555556
	s_mul_i32 s14, s13, 3
	s_sub_i32 s14, s12, s14
	s_add_i32 s15, s13, s6
	s_cmp_eq_u32 s14, 0
	s_cbranch_scc0 .Lln2st_k9
	s_mul_i32 s16, s15, 0x6000
	s_add_u32 s16, s16, 0x105000
	s_add_u32 s20, s0, s16
	s_addc_u32 s21, s1, 0
	global_load_dwordx4 v[52:55], v10, s[20:21]
	s_branch .Lln2st_n9
.Lln2st_k9:
	v_mov_b32_e32 v52, 0
	v_mov_b32_e32 v53, 0
	v_mov_b32_e32 v54, 0
	v_mov_b32_e32 v55, 0
	s_and_b64 vcc, exec, s[22:23]
	s_cbranch_vccz .Lln2st_n9
	s_add_i32 s15, s15, 9
	s_mul_i32 s16, s15, 6
	s_cmp_eq_u32 s14, 1
	s_cselect_b32 s17, 1, 0
	s_or_b32 s16, s16, s17
	s_lshl_b32 s16, s16, 12
	s_add_u32 s20, s8, s16
	s_addc_u32 s21, s9, 0
	global_load_dwordx4 v[52:55], v10, s[20:21]
.Lln2st_n9:
	s_add_i32 s12, s7, 20
	s_mul_hi_u32 s13, s12, 0x55555556
	s_mul_i32 s14, s13, 3
	s_sub_i32 s14, s12, s14
	s_add_i32 s15, s13, s6
	s_cmp_eq_u32 s14, 0
	s_cbranch_scc0 .Lln2st_k10
	s_mul_i32 s16, s15, 0x6000
	s_add_u32 s16, s16, 0x105000
	s_add_u32 s20, s0, s16
	s_addc_u32 s21, s1, 0
	global_load_dwordx4 v[56:59], v10, s[20:21]
	s_branch .Lln2st_n10
.Lln2st_k10:
	v_mov_b32_e32 v56, 0
	v_mov_b32_e32 v57, 0
	v_mov_b32_e32 v58, 0
	v_mov_b32_e32 v59, 0
	s_and_b64 vcc, exec, s[22:23]
	s_cbranch_vccz .Lln2st_n10
	s_add_i32 s15, s15, 9
	s_mul_i32 s16, s15, 6
	s_cmp_eq_u32 s14, 1
	s_cselect_b32 s17, 1, 0
	s_or_b32 s16, s16, s17
	s_lshl_b32 s16, s16, 12
	s_add_u32 s20, s8, s16
	s_addc_u32 s21, s9, 0
	global_load_dwordx4 v[56:59], v10, s[20:21]
; #define LAS __attribute__((address_space(3)))
; __device__ __forceinline__ const float* modv(const Frame& F, int l, int r, int k) { return (const float*)(F.ws + WS_MODV) + ((size_t)(l * 9 + r) * 6 + k) * 1024; }
; __device__ __forceinline__ void phase_ln2(Frame& F0, const Args& A, int l, bool have_moe) {
;     ...
;     for (int i = F.tid; i < 27 * 256; i += 512) { const int r = i / 768, k = (i / 256) % 3, c = (i & 255) * 4;
;         const f32x4 v = (k == 0) ? *(const f32x4*)(modv(F, l, r, 5) + c) : (last ? (f32x4){0.f, 0.f, 0.f, 0.f} : *(const f32x4*)(modv(F, l + 1, r, k == 1 ? 1 : 0) + c));
;         *(LAS f32x4*)(MV + (r * 3 + k) * 1024 + c) = v; }
;     for (int i = F.tid; i < 256; i += 512) { *(LAS f32x4*)(LG + i * 4) = *(const f32x4*)(lg + i * 4); *(LAS f32x4*)(LB + i * 4) = *(const f32x4*)(lb + i * 4); }
.Lln2st_n10:
	s_add_i32 s12, s7, 22
	s_mul_hi_u32 s13, s12, 0x55555556
	s_mul_i32 s14, s13, 3
	s_sub_i32 s14, s12, s14
	s_add_i32 s15, s13, s6
	s_cmp_eq_u32 s14, 0
	s_cbranch_scc0 .Lln2st_k11
	s_mul_i32 s16, s15, 0x6000
	s_add_u32 s16, s16, 0x105000
	s_add_u32 s20, s0, s16
	s_addc_u32 s21, s1, 0
	global_load_dwordx4 v[60:63], v10, s[20:21]
	s_branch .Lln2st_n11
.Lln2st_k11:
	v_mov_b32_e32 v60, 0
	v_mov_b32_e32 v61, 0
	v_mov_b32_e32 v62, 0
	v_mov_b32_e32 v63, 0
	s_and_b64 vcc, exec, s[22:23]
	s_cbranch_vccz .Lln2st_n11
	s_add_i32 s15, s15, 9
	s_mul_i32 s16, s15, 6
	s_cmp_eq_u32 s14, 1
	s_cselect_b32 s17, 1, 0
	s_or_b32 s16, s16, s17
	s_lshl_b32 s16, s16, 12
	s_add_u32 s20, s8, s16
	s_addc_u32 s21, s9, 0
	global_load_dwordx4 v[60:63], v10, s[20:21]
.Lln2st_n11:
	s_add_i32 s12, s7, 24
	s_mul_hi_u32 s13, s12, 0x55555556
	s_mul_i32 s14, s13, 3
	s_sub_i32 s14, s12, s14
	s_add_i32 s15, s13, s6
	s_cmp_eq_u32 s14, 0
	s_cbranch_scc0 .Lln2st_k12
	s_mul_i32 s16, s15, 0x6000
	s_add_u32 s16, s16, 0x105000
	s_add_u32 s20, s0, s16
	s_addc_u32 s21, s1, 0
	global_load_dwordx4 v[64:67], v10, s[20:21]
	s_branch .Lln2st_n12
.Lln2st_k12:
	v_mov_b32_e32 v64, 0
	v_mov_b32_e32 v65, 0
	v_mov_b32_e32 v66, 0
	v_mov_b32_e32 v67, 0
	s_and_b64 vcc, exec, s[22:23]
	s_cbranch_vccz .Lln2st_n12
	s_add_i32 s15, s15, 9
	s_mul_i32 s16, s15, 6
	s_cmp_eq_u32 s14, 1
	s_cselect_b32 s17, 1, 0
	s_or_b32 s16, s16, s17
	s_lshl_b32 s16, s16, 12
	s_add_u32 s20, s8, s16
	s_addc_u32 s21, s9, 0
	global_load_dwordx4 v[64:67], v10, s[20:21]
.Lln2st_n12:
	s_add_i32 s12, s7, 26
	s_cmp_ge_u32 s12, 27
	s_cbranch_scc1 .Lln2st_wait
	s_mul_hi_u32 s13, s12, 0x55555556
	s_mul_i32 s14, s13, 3
	s_sub_i32 s14, s12, s14
	s_add_i32 s15, s13, s6
	s_cmp_eq_u32 s14, 0
	s_cbranch_scc0 .Lln2st_k13
	s_mul_i32 s16, s15, 0x6000
	s_add_u32 s16, s16, 0x105000
	s_add_u32 s20, s0, s16
	s_addc_u32 s21, s1, 0
	global_load_dwordx4 v[68:71], v10, s[20:21]
	s_branch .Lln2st_n13
.Lln2st_k13:
	v_mov_b32_e32 v68, 0
	v_mov_b32_e32 v69, 0
	v_mov_b32_e32 v70, 0
	v_mov_b32_e32 v71, 0
	s_and_b64 vcc, exec, s[22:23]
	s_cbranch_vccz .Lln2st_n13
	s_add_i32 s15, s15, 9
	s_mul_i32 s16, s15, 6
	s_cmp_eq_u32 s14, 1
	s_cselect_b32 s17, 1, 0
	s_or_b32 s16, s16, s17
	s_lshl_b32 s16, s16, 12
	s_add_u32 s20, s8, s16
	s_addc_u32 s21, s9, 0
	global_load_dwordx4 v[68:71], v10, s[20:21]
.Lln2st_n13:
.Lln2st_wait:
	s_waitcnt vmcnt(0)
	ds_write_b128 v11, v[16:19]
	ds_write_b128 v11, v[20:23] offset:8192
	ds_write_b128 v11, v[24:27] offset:16384
	ds_write_b128 v11, v[28:31] offset:24576
	ds_write_b128 v11, v[32:35] offset:32768
	ds_write_b128 v11, v[36:39] offset:40960
	ds_write_b128 v11, v[40:43] offset:49152
	ds_write_b128 v11, v[44:47] offset:57344
	ds_write_b128 v12, v[48:51]
	ds_write_b128 v12, v[52:55] offset:8192
	ds_write_b128 v12, v[56:59] offset:16384
	ds_write_b128 v12, v[60:63] offset:24576
	ds_write_b128 v12, v[64:67] offset:32768
	s_cmp_lg_u32 s7, 0
	s_cbranch_scc1 .Lln2st_done
	ds_write_b128 v12, v[68:71] offset:40960
.Lln2st_done:
.LBB0_1704:
	s_or_b64 exec, exec, s[4:5]
	s_movk_i32 s4, 0x100
	v_lshlrev_b32_e32 v136, 4, v156
	v_cmp_gt_i32_e32 vcc, s4, v5
	s_and_saveexec_b64 s[4:5], vcc
	s_cbranch_execz .LBB0_1707
	v_readlane_b32 s6, v254, 56
	v_readlane_b32 s7, v254, 57
	s_waitcnt lgkmcnt(0)
	s_add_u32 s8, s36, s6
	s_addc_u32 s9, s37, s7
	s_add_u32 s12, s38, s6
	s_addc_u32 s13, s39, s7
	s_lshl_b32 s6, s18, 10
	s_add_i32 s6, s6, 0
	v_add_u32_e32 v0, s19, v156
	s_add_i32 s6, s6, 0x1c000
	v_add_u32_e32 v0, 0xfffffe00, v0
	v_add_u32_e32 v1, s6, v136
	s_mov_b64 s[14:15], 0
